# speedup vs baseline: 1.0414x; 1.0029x over previous
.LBB1_233:
	s_or_b64 exec, exec, s[4:5]
	v_min_i32_e32 v2, v14, v25
	v_cmp_gt_i32_e32 vcc, v2, v0
	s_waitcnt lgkmcnt(0)
	s_barrier
	s_and_saveexec_b64 s[2:3], vcc
	s_cbranch_execz .LBB1_242
	v_min_i32_e32 v4, 0x2000, v2
	v_add_u32_e32 v4, 3, v4
	v_ashrrev_i32_e32 v4, 2, v4
	v_cmp_lt_i32_e32 vcc, v0, v4
	s_and_b64 exec, exec, vcc
	s_cbranch_execz .LBB1_242
	v_lshlrev_b32_e32 v1, 4, v0
	ds_read_b128 v[6:9], v1
	ds_read_b128 v[14:17], v1 offset:16384
	s_lshr_b32 s4, s56, 2
	v_or_b32_e32 v2, s4, v0
	v_mov_b32_e32 v3, 0
	v_lshl_add_u64 v[10:11], v[2:3], 4, s[52:53]
	v_or_b32_e32 v5, 0x400, v0
	v_cmp_lt_i32_e32 vcc, v5, v4
	v_add_u32_e32 v2, 0x400, v2
	v_lshl_add_u64 v[12:13], v[2:3], 4, s[52:53]
	s_waitcnt lgkmcnt(1)
	global_store_dwordx4 v[10:11], v[6:9], off
	s_and_b64 exec, exec, vcc
	s_cbranch_execz .LBB1_242
	s_waitcnt lgkmcnt(0)
	global_store_dwordx4 v[12:13], v[14:17], off
